# stack14 plus rowmax cross-half permlane moved from common path into the rare rescale blocks (per-lane partial max check is equivalent)
# baseline (speedup 1.0000x reference)
; #define AT_SBAR() __builtin_amdgcn_sched_barrier(0)
; template <int OFF> DI s16x4 tr_read(int vb) { s16x4 r; asm volatile("ds_read_b64_tr_b16 %0, %1 offset:%2" : "=&v"(r) : "v"(vb), "i"(OFF) : "memory"); return r; }
; template <int D0> DI void pv_one(f32x16& od, int vb, bf16x8 pa0, bf16x8 pa1, bf16x8 pa2, bf16x8 pa3) {
;     const s16x4 l0 = tr_read<v_rd_off(D0, 0, 0)>(vb), h0 = tr_read<v_rd_off(D0, 0, 1)>(vb), l1 = tr_read<v_rd_off(D0, 1, 0)>(vb), h1 = tr_read<v_rd_off(D0, 1, 1)>(vb);
;     const s16x4 l2 = tr_read<v_rd_off(D0, 2, 0)>(vb), h2 = tr_read<v_rd_off(D0, 2, 1)>(vb), l3 = tr_read<v_rd_off(D0, 3, 0)>(vb), h3 = tr_read<v_rd_off(D0, 3, 1)>(vb);
;     asm volatile("s_waitcnt lgkmcnt(0)" ::: "memory"); AT_SBAR();
;     ...
;     od = __builtin_amdgcn_mfma_f32_32x32x16_bf16(AT_PK(l0, h0), pa0, od, 0, 0, 0);
;     od = __builtin_amdgcn_mfma_f32_32x32x16_bf16(AT_PK(l1, h1), pa1, od, 0, 0, 0);
;     od = __builtin_amdgcn_mfma_f32_32x32x16_bf16(AT_PK(l2, h2), pa2, od, 0, 0, 0);
;     od = __builtin_amdgcn_mfma_f32_32x32x16_bf16(AT_PK(l3, h3), pa3, od, 0, 0, 0);
;     ...
; }
; DI void pv_all_sm(f32x16* o, int vb, bf16x8 pa0, bf16x8 pa1, bf16x8 pa2, bf16x8 pa3, f32x16& p0, f32x16& p1, float& m_ref, f32x16& negm, float& alpha) {
;     pv_one<0>(o[0], vb, pa0, pa1, pa2, pa3);
;     float pmax = p0[0];
; #pragma unroll
;     for (int r = 1; r < 16; ++r) pmax = fmaxf(pmax, p0[r]);
;     pv_one<1>(o[1], vb, pa0, pa1, pa2, pa3);
; #pragma unroll
;     for (int r = 0; r < 16; ++r) pmax = fmaxf(pmax, p1[r]);
;     { auto rr = __builtin_amdgcn_permlane32_swap(__float_as_uint(pmax), __float_as_uint(pmax), false, false); pmax = fmaxf(__uint_as_float(rr[0]), __uint_as_float(rr[1])); }
;     pv_one<2>(o[2], vb, pa0, pa1, pa2, pa3);
;     alpha = 1.f;
;     if (__builtin_expect(!__all(pmax <= THRL), 0)) {
;         const float dl = fmaxf(pmax, 0.f); m_ref += dl; alpha = __builtin_amdgcn_exp2f(-dl);
; #pragma unroll
;         for (int r = 0; r < 16; ++r) { p0[r] -= dl; p1[r] -= dl; }
; #pragma unroll
;         for (int r = 0; r < 16; ++r) negm[r] = -m_ref;
;     }
.LBB4_704:
	s_lshl_b32 s67, s65, 14
	v_add_u32_e32 v186, s67, v253
	ds_read_b64_tr_b16 v[64:65], v186 offset:0
	ds_read_b64_tr_b16 v[66:67], v186 offset:0x100
	ds_read_b64_tr_b16 v[68:69], v186 offset:0x1000
	ds_read_b64_tr_b16 v[70:71], v186 offset:0x1100
	ds_read_b64_tr_b16 v[72:73], v186 offset:0x2000
	ds_read_b64_tr_b16 v[74:75], v186 offset:0x2100
	ds_read_b64_tr_b16 v[76:77], v186 offset:0x3000
	ds_read_b64_tr_b16 v[78:79], v186 offset:0x3100
	s_waitcnt lgkmcnt(0)
	v_mfma_f32_32x32x16_bf16 v[32:47], v[64:67], v[96:99], v[32:47]
	v_max_f32_e32 v64, v128, v129
	v_max3_f32 v64, v64, v130, v131
	v_max3_f32 v64, v64, v132, v133
	v_max3_f32 v64, v64, v134, v135
	v_max3_f32 v64, v64, v136, v137
	v_mfma_f32_32x32x16_bf16 v[32:47], v[68:71], v[108:111], v[32:47]
	v_max3_f32 v64, v64, v138, v139
	v_max3_f32 v66, v64, v140, v141
	ds_read_b64_tr_b16 v[64:65], v186 offset:0x200
	v_max3_f32 v180, v66, v142, v143
	ds_read_b64_tr_b16 v[66:67], v186 offset:0x300
	ds_read_b64_tr_b16 v[68:69], v186 offset:0x1200
	ds_read_b64_tr_b16 v[70:71], v186 offset:0x1300
	v_mfma_f32_32x32x16_bf16 v[32:47], v[72:75], v[100:103], v[32:47]
	ds_read_b64_tr_b16 v[72:73], v186 offset:0x2200
	ds_read_b64_tr_b16 v[74:75], v186 offset:0x2300
	ds_read_b64_tr_b16 v[214:215], v186 offset:0x3200
	ds_read_b64_tr_b16 v[216:217], v186 offset:0x3300
	v_mfma_f32_32x32x16_bf16 v[32:47], v[76:79], v[104:107], v[32:47]
	s_waitcnt lgkmcnt(0)
	v_mfma_f32_32x32x16_bf16 v[48:63], v[64:67], v[96:99], v[48:63]
	v_max3_f32 v76, v180, v112, v113
	v_max3_f32 v64, v76, v114, v115
	ds_read_b64_tr_b16 v[66:67], v186 offset:0x400
	v_max3_f32 v64, v64, v116, v117
	v_max3_f32 v64, v64, v118, v119
	v_max3_f32 v64, v64, v120, v121
	v_max3_f32 v64, v64, v122, v123
	v_mfma_f32_32x32x16_bf16 v[48:63], v[68:71], v[108:111], v[48:63]
	ds_read_b64_tr_b16 v[68:69], v186 offset:0x500
	ds_read_b64_tr_b16 v[70:71], v186 offset:0x1400
	v_max3_f32 v64, v64, v124, v125
	v_max3_f32 v64, v64, v126, v127
	v_mfma_f32_32x32x16_bf16 v[48:63], v[72:75], v[100:103], v[48:63]
	ds_read_b64_tr_b16 v[72:73], v186 offset:0x1500
	ds_read_b64_tr_b16 v[74:75], v186 offset:0x2400
	ds_read_b64_tr_b16 v[76:77], v186 offset:0x2500
	ds_read_b64_tr_b16 v[218:219], v186 offset:0x3400
	ds_read_b64_tr_b16 v[220:221], v186 offset:0x3500
	v_mfma_f32_32x32x16_bf16 v[48:63], v[214:217], v[104:107], v[48:63]
	s_waitcnt lgkmcnt(0)
	v_mfma_f32_32x32x16_bf16 v[16:31], v[66:69], v[96:99], v[16:31]
	v_cmp_ge_f32_e32 vcc, s25, v64
	s_cmp_eq_u64 vcc, exec
	v_mfma_f32_32x32x16_bf16 v[16:31], v[70:73], v[108:111], v[16:31]
	v_mfma_f32_32x32x16_bf16 v[16:31], v[74:77], v[100:103], v[16:31]
	v_mfma_f32_32x32x16_bf16 v[16:31], v[218:221], v[104:107], v[16:31]
	s_cbranch_scc0 .LBB4_737
	v_mov_b32_e32 v180, 1.0

; #define AT_SBAR() __builtin_amdgcn_sched_barrier(0)
; template <int OFF> DI s16x4 tr_read(int vb) { s16x4 r; asm volatile("ds_read_b64_tr_b16 %0, %1 offset:%2" : "=&v"(r) : "v"(vb), "i"(OFF) : "memory"); return r; }
; template <int D0> DI void pv_one(f32x16& od, int vb, bf16x8 pa0, bf16x8 pa1, bf16x8 pa2, bf16x8 pa3) {
;     const s16x4 l0 = tr_read<v_rd_off(D0, 0, 0)>(vb), h0 = tr_read<v_rd_off(D0, 0, 1)>(vb), l1 = tr_read<v_rd_off(D0, 1, 0)>(vb), h1 = tr_read<v_rd_off(D0, 1, 1)>(vb);
;     const s16x4 l2 = tr_read<v_rd_off(D0, 2, 0)>(vb), h2 = tr_read<v_rd_off(D0, 2, 1)>(vb), l3 = tr_read<v_rd_off(D0, 3, 0)>(vb), h3 = tr_read<v_rd_off(D0, 3, 1)>(vb);
;     asm volatile("s_waitcnt lgkmcnt(0)" ::: "memory"); AT_SBAR();
;     ...
;     od = __builtin_amdgcn_mfma_f32_32x32x16_bf16(AT_PK(l0, h0), pa0, od, 0, 0, 0);
;     od = __builtin_amdgcn_mfma_f32_32x32x16_bf16(AT_PK(l1, h1), pa1, od, 0, 0, 0);
;     od = __builtin_amdgcn_mfma_f32_32x32x16_bf16(AT_PK(l2, h2), pa2, od, 0, 0, 0);
;     od = __builtin_amdgcn_mfma_f32_32x32x16_bf16(AT_PK(l3, h3), pa3, od, 0, 0, 0);
;     ...
; }
; DI void pv_all_sm(f32x16* o, int vb, bf16x8 pa0, bf16x8 pa1, bf16x8 pa2, bf16x8 pa3, f32x16& p0, f32x16& p1, float& m_ref, f32x16& negm, float& alpha) {
;     pv_one<0>(o[0], vb, pa0, pa1, pa2, pa3);
;     float pmax = p0[0];
; #pragma unroll
;     for (int r = 1; r < 16; ++r) pmax = fmaxf(pmax, p0[r]);
;     pv_one<1>(o[1], vb, pa0, pa1, pa2, pa3);
; #pragma unroll
;     for (int r = 0; r < 16; ++r) pmax = fmaxf(pmax, p1[r]);
;     { auto rr = __builtin_amdgcn_permlane32_swap(__float_as_uint(pmax), __float_as_uint(pmax), false, false); pmax = fmaxf(__uint_as_float(rr[0]), __uint_as_float(rr[1])); }
;     pv_one<2>(o[2], vb, pa0, pa1, pa2, pa3);
;     alpha = 1.f;
;     if (__builtin_expect(!__all(pmax <= THRL), 0)) {
;         const float dl = fmaxf(pmax, 0.f); m_ref += dl; alpha = __builtin_amdgcn_exp2f(-dl);
; #pragma unroll
;         for (int r = 0; r < 16; ++r) { p0[r] -= dl; p1[r] -= dl; }
; #pragma unroll
;         for (int r = 0; r < 16; ++r) negm[r] = -m_ref;
;     }
.LBB4_725:
	v_lshl_add_u32 v215, s66, 14, v253
	ds_read_b64_tr_b16 v[216:217], v215 offset:0
	ds_read_b64_tr_b16 v[218:219], v215 offset:0x100
	ds_read_b64_tr_b16 v[220:221], v215 offset:0x1000
	ds_read_b64_tr_b16 v[222:223], v215 offset:0x1100
	ds_read_b64_tr_b16 v[224:225], v215 offset:0x2000
	ds_read_b64_tr_b16 v[226:227], v215 offset:0x2100
	ds_read_b64_tr_b16 v[228:229], v215 offset:0x3000
	ds_read_b64_tr_b16 v[230:231], v215 offset:0x3100
	s_waitcnt lgkmcnt(0)
	v_mfma_f32_32x32x16_bf16 v[32:47], v[216:219], v[120:123], v[32:47]
	v_max_f32_e32 v186, v128, v129
	ds_read_b64_tr_b16 v[216:217], v215 offset:0x200
	ds_read_b64_tr_b16 v[218:219], v215 offset:0x300
	v_max3_f32 v186, v186, v130, v131
	v_max3_f32 v186, v186, v132, v133
	v_mfma_f32_32x32x16_bf16 v[32:47], v[220:223], v[124:127], v[32:47]
	ds_read_b64_tr_b16 v[220:221], v215 offset:0x1200
	ds_read_b64_tr_b16 v[222:223], v215 offset:0x1300
	v_max3_f32 v186, v186, v134, v135
	v_max3_f32 v186, v186, v136, v137
	v_max3_f32 v186, v186, v138, v139
	v_max3_f32 v186, v186, v140, v141
	v_max3_f32 v186, v186, v142, v143
	v_mfma_f32_32x32x16_bf16 v[32:47], v[224:227], v[112:115], v[32:47]
	ds_read_b64_tr_b16 v[224:225], v215 offset:0x2200
	ds_read_b64_tr_b16 v[226:227], v215 offset:0x2300
	ds_read_b64_tr_b16 v[232:233], v215 offset:0x3200
	ds_read_b64_tr_b16 v[234:235], v215 offset:0x3300
	v_mfma_f32_32x32x16_bf16 v[32:47], v[228:231], v[116:119], v[32:47]
	s_waitcnt lgkmcnt(0)
	v_mfma_f32_32x32x16_bf16 v[48:63], v[216:219], v[120:123], v[48:63]
	v_max3_f32 v186, v186, v96, v97
	v_max3_f32 v186, v186, v98, v99
	ds_read_b64_tr_b16 v[218:219], v215 offset:0x400
	v_max3_f32 v186, v186, v100, v101
	v_max3_f32 v186, v186, v102, v103
	v_max3_f32 v186, v186, v104, v105
	v_max3_f32 v186, v186, v106, v107
	v_mfma_f32_32x32x16_bf16 v[48:63], v[220:223], v[124:127], v[48:63]
	ds_read_b64_tr_b16 v[220:221], v215 offset:0x500
	ds_read_b64_tr_b16 v[222:223], v215 offset:0x1400
	v_max3_f32 v186, v186, v108, v109
	v_max3_f32 v186, v186, v110, v111
	v_mov_b32_e32 v216, v186
	v_mfma_f32_32x32x16_bf16 v[48:63], v[224:227], v[112:115], v[48:63]
	ds_read_b64_tr_b16 v[224:225], v215 offset:0x1500
	ds_read_b64_tr_b16 v[226:227], v215 offset:0x2400
	ds_read_b64_tr_b16 v[228:229], v215 offset:0x2500
	ds_read_b64_tr_b16 v[236:237], v215 offset:0x3400
	ds_read_b64_tr_b16 v[238:239], v215 offset:0x3500
	v_mfma_f32_32x32x16_bf16 v[48:63], v[232:235], v[116:119], v[48:63]
	s_waitcnt lgkmcnt(0)
	v_mfma_f32_32x32x16_bf16 v[16:31], v[218:221], v[120:123], v[16:31]
	v_cmp_ge_f32_e32 vcc, s25, v216
	s_cmp_eq_u64 vcc, exec
	v_mov_b32_e32 v186, 1.0
	v_mfma_f32_32x32x16_bf16 v[16:31], v[222:225], v[124:127], v[16:31]
	v_mfma_f32_32x32x16_bf16 v[16:31], v[226:229], v[112:115], v[16:31]
	v_mfma_f32_32x32x16_bf16 v[16:31], v[236:239], v[116:119], v[16:31]
	s_cbranch_scc0 .LBB4_738

; DI void pv_all_sm(f32x16* o, int vb, bf16x8 pa0, bf16x8 pa1, bf16x8 pa2, bf16x8 pa3, f32x16& p0, f32x16& p1, float& m_ref, f32x16& negm, float& alpha) {
;     ...
;     { auto rr = __builtin_amdgcn_permlane32_swap(__float_as_uint(pmax), __float_as_uint(pmax), false, false); pmax = fmaxf(__uint_as_float(rr[0]), __uint_as_float(rr[1])); }
;     pv_one<2>(o[2], vb, pa0, pa1, pa2, pa3);
;     alpha = 1.f;
;     if (__builtin_expect(!__all(pmax <= THRL), 0)) {
;         const float dl = fmaxf(pmax, 0.f); m_ref += dl; alpha = __builtin_amdgcn_exp2f(-dl);
; #pragma unroll
;         for (int r = 0; r < 16; ++r) { p0[r] -= dl; p1[r] -= dl; }
; #pragma unroll
;         for (int r = 0; r < 16; ++r) negm[r] = -m_ref;
;     }
.LBB4_737:
	v_mov_b32_e32 v65, v64
	s_nop 1
	v_permlane32_swap_b32_e32 v64, v65
	v_max_f32_e32 v64, v64, v65
	v_max_f32_e32 v64, v64, v64
	v_max_f32_e32 v64, 0, v64
	v_exp_f32_e64 v180, -v64
	v_add_f32_e32 v208, v208, v64
	v_pk_add_f32 v[128:129], v[128:129], v[64:65] op_sel_hi:[1,0] neg_lo:[0,1] neg_hi:[0,1]
	v_pk_add_f32 v[130:131], v[130:131], v[64:65] op_sel_hi:[1,0] neg_lo:[0,1] neg_hi:[0,1]
	v_pk_add_f32 v[132:133], v[132:133], v[64:65] op_sel_hi:[1,0] neg_lo:[0,1] neg_hi:[0,1]
	v_pk_add_f32 v[134:135], v[134:135], v[64:65] op_sel_hi:[1,0] neg_lo:[0,1] neg_hi:[0,1]
	v_pk_add_f32 v[136:137], v[136:137], v[64:65] op_sel_hi:[1,0] neg_lo:[0,1] neg_hi:[0,1]
	v_pk_add_f32 v[138:139], v[138:139], v[64:65] op_sel_hi:[1,0] neg_lo:[0,1] neg_hi:[0,1]
	v_pk_add_f32 v[140:141], v[140:141], v[64:65] op_sel_hi:[1,0] neg_lo:[0,1] neg_hi:[0,1]
	v_pk_add_f32 v[142:143], v[142:143], v[64:65] op_sel_hi:[1,0] neg_lo:[0,1] neg_hi:[0,1]
	v_sub_f32_e32 v127, v127, v64
	v_sub_f32_e32 v126, v126, v64
	v_sub_f32_e32 v125, v125, v64
	v_sub_f32_e32 v124, v124, v64
	v_sub_f32_e32 v123, v123, v64
	v_sub_f32_e32 v122, v122, v64
	v_sub_f32_e32 v121, v121, v64
	v_sub_f32_e32 v120, v120, v64
	v_sub_f32_e32 v119, v119, v64
	v_sub_f32_e32 v118, v118, v64
	v_sub_f32_e32 v117, v117, v64
	v_sub_f32_e32 v116, v116, v64
	v_sub_f32_e32 v115, v115, v64
	v_sub_f32_e32 v114, v114, v64
	v_sub_f32_e32 v113, v113, v64
	v_sub_f32_e32 v112, v112, v64
	v_xor_b32_e32 v64, 0x80000000, v208
	v_mov_b32_e32 v65, v64
	v_mov_b32_e32 v66, v64
	v_mov_b32_e32 v67, v64
	v_mov_b32_e32 v68, v64
	v_mov_b32_e32 v69, v64
	v_mov_b32_e32 v70, v64
	v_mov_b32_e32 v71, v64
	v_mov_b32_e32 v72, v64
	v_mov_b32_e32 v73, v64
	v_mov_b32_e32 v74, v64
	v_mov_b32_e32 v75, v64
	v_mov_b32_e32 v76, v64
	v_mov_b32_e32 v77, v64
	v_mov_b32_e32 v78, v64
	v_mov_b32_e32 v79, v64
	v_mov_b32_e32 v80, v64
	v_mov_b32_e32 v81, v64
	v_mov_b32_e32 v82, v64
	v_mov_b32_e32 v83, v64
	v_mov_b32_e32 v84, v64
	v_mov_b32_e32 v85, v64
	v_mov_b32_e32 v86, v64
	v_mov_b32_e32 v87, v64
	v_mov_b32_e32 v88, v64
	v_mov_b32_e32 v89, v64
	v_mov_b32_e32 v90, v64
	v_mov_b32_e32 v91, v64
	v_mov_b32_e32 v92, v64
	v_mov_b32_e32 v93, v64
	v_mov_b32_e32 v94, v64
	v_mov_b32_e32 v95, v64
	s_branch .LBB4_706
.LBB4_738:
	v_mov_b32_e32 v254, v216
	s_nop 1
	v_permlane32_swap_b32_e32 v216, v254
	v_max_f32_e32 v216, v216, v254
	v_max_f32_e32 v64, v216, v216
	v_max_f32_e32 v64, 0, v64
	v_exp_f32_e64 v186, -v64
	v_add_f32_e32 v208, v208, v64
	v_pk_add_f32 v[128:129], v[128:129], v[64:65] op_sel_hi:[1,0] neg_lo:[0,1] neg_hi:[0,1]
	v_pk_add_f32 v[130:131], v[130:131], v[64:65] op_sel_hi:[1,0] neg_lo:[0,1] neg_hi:[0,1]
	v_pk_add_f32 v[132:133], v[132:133], v[64:65] op_sel_hi:[1,0] neg_lo:[0,1] neg_hi:[0,1]
	v_pk_add_f32 v[134:135], v[134:135], v[64:65] op_sel_hi:[1,0] neg_lo:[0,1] neg_hi:[0,1]
	v_pk_add_f32 v[136:137], v[136:137], v[64:65] op_sel_hi:[1,0] neg_lo:[0,1] neg_hi:[0,1]
	v_pk_add_f32 v[138:139], v[138:139], v[64:65] op_sel_hi:[1,0] neg_lo:[0,1] neg_hi:[0,1]
	v_pk_add_f32 v[140:141], v[140:141], v[64:65] op_sel_hi:[1,0] neg_lo:[0,1] neg_hi:[0,1]
	v_pk_add_f32 v[142:143], v[142:143], v[64:65] op_sel_hi:[1,0] neg_lo:[0,1] neg_hi:[0,1]
	v_sub_f32_e32 v111, v111, v64
	v_sub_f32_e32 v110, v110, v64
	v_sub_f32_e32 v109, v109, v64
	v_sub_f32_e32 v108, v108, v64
	v_sub_f32_e32 v107, v107, v64
	v_sub_f32_e32 v106, v106, v64
	v_sub_f32_e32 v105, v105, v64
	v_sub_f32_e32 v104, v104, v64
	v_sub_f32_e32 v103, v103, v64
	v_sub_f32_e32 v102, v102, v64
	v_sub_f32_e32 v101, v101, v64
	v_sub_f32_e32 v100, v100, v64
	v_sub_f32_e32 v99, v99, v64
	v_sub_f32_e32 v98, v98, v64
	v_sub_f32_e32 v97, v97, v64
	v_sub_f32_e32 v96, v96, v64
	v_xor_b32_e32 v64, 0x80000000, v208
	v_mov_b32_e32 v65, v64
	v_mov_b32_e32 v66, v64
	v_mov_b32_e32 v67, v64
	v_mov_b32_e32 v68, v64
	v_mov_b32_e32 v69, v64
	v_mov_b32_e32 v70, v64
	v_mov_b32_e32 v71, v64
	v_mov_b32_e32 v72, v64
	v_mov_b32_e32 v73, v64
	v_mov_b32_e32 v74, v64
	v_mov_b32_e32 v75, v64
	v_mov_b32_e32 v76, v64
	v_mov_b32_e32 v77, v64
	v_mov_b32_e32 v78, v64
	v_mov_b32_e32 v79, v64
	v_mov_b32_e32 v80, v64
	v_mov_b32_e32 v81, v64
	v_mov_b32_e32 v82, v64
	v_mov_b32_e32 v83, v64
	v_mov_b32_e32 v84, v64
	v_mov_b32_e32 v85, v64
	v_mov_b32_e32 v86, v64
	v_mov_b32_e32 v87, v64
	v_mov_b32_e32 v88, v64
	v_mov_b32_e32 v89, v64
	v_mov_b32_e32 v90, v64
	v_mov_b32_e32 v91, v64
	v_mov_b32_e32 v92, v64
	v_mov_b32_e32 v93, v64
	v_mov_b32_e32 v94, v64
	v_mov_b32_e32 v95, v64
	s_branch .LBB4_726

; #define AT_SBAR() __builtin_amdgcn_sched_barrier(0)
; template <int OFF> DI s16x4 tr_read(int vb) { s16x4 r; asm volatile("ds_read_b64_tr_b16 %0, %1 offset:%2" : "=&v"(r) : "v"(vb), "i"(OFF) : "memory"); return r; }
; template <int D0> DI void pv_one(f32x16& od, int vb, bf16x8 pa0, bf16x8 pa1, bf16x8 pa2, bf16x8 pa3) {
;     const s16x4 l0 = tr_read<v_rd_off(D0, 0, 0)>(vb), h0 = tr_read<v_rd_off(D0, 0, 1)>(vb), l1 = tr_read<v_rd_off(D0, 1, 0)>(vb), h1 = tr_read<v_rd_off(D0, 1, 1)>(vb);
;     const s16x4 l2 = tr_read<v_rd_off(D0, 2, 0)>(vb), h2 = tr_read<v_rd_off(D0, 2, 1)>(vb), l3 = tr_read<v_rd_off(D0, 3, 0)>(vb), h3 = tr_read<v_rd_off(D0, 3, 1)>(vb);
;     asm volatile("s_waitcnt lgkmcnt(0)" ::: "memory"); AT_SBAR();
;     ...
;     od = __builtin_amdgcn_mfma_f32_32x32x16_bf16(AT_PK(l0, h0), pa0, od, 0, 0, 0);
;     od = __builtin_amdgcn_mfma_f32_32x32x16_bf16(AT_PK(l1, h1), pa1, od, 0, 0, 0);
;     od = __builtin_amdgcn_mfma_f32_32x32x16_bf16(AT_PK(l2, h2), pa2, od, 0, 0, 0);
;     od = __builtin_amdgcn_mfma_f32_32x32x16_bf16(AT_PK(l3, h3), pa3, od, 0, 0, 0);
;     ...
; }
; DI void pv_all_sm(f32x16* o, int vb, bf16x8 pa0, bf16x8 pa1, bf16x8 pa2, bf16x8 pa3, f32x16& p0, f32x16& p1, float& m_ref, f32x16& negm, float& alpha) {
;     pv_one<0>(o[0], vb, pa0, pa1, pa2, pa3);
;     float pmax = p0[0];
; #pragma unroll
;     for (int r = 1; r < 16; ++r) pmax = fmaxf(pmax, p0[r]);
;     pv_one<1>(o[1], vb, pa0, pa1, pa2, pa3);
; #pragma unroll
;     for (int r = 0; r < 16; ++r) pmax = fmaxf(pmax, p1[r]);
;     { auto rr = __builtin_amdgcn_permlane32_swap(__float_as_uint(pmax), __float_as_uint(pmax), false, false); pmax = fmaxf(__uint_as_float(rr[0]), __uint_as_float(rr[1])); }
;     pv_one<2>(o[2], vb, pa0, pa1, pa2, pa3);
;     alpha = 1.f;
;     if (__builtin_expect(!__all(pmax <= THRL), 0)) {
;         const float dl = fmaxf(pmax, 0.f); m_ref += dl; alpha = __builtin_amdgcn_exp2f(-dl);
; #pragma unroll
;         for (int r = 0; r < 16; ++r) { p0[r] -= dl; p1[r] -= dl; }
; #pragma unroll
;         for (int r = 0; r < 16; ++r) negm[r] = -m_ref;
;     }
.LBB4_777:
	s_lshl_b32 s31, s29, 14
	v_add_u32_e32 v182, s31, v253
	ds_read_b64_tr_b16 v[64:65], v182 offset:0
	ds_read_b64_tr_b16 v[66:67], v182 offset:0x100
	ds_read_b64_tr_b16 v[68:69], v182 offset:0x1000
	ds_read_b64_tr_b16 v[70:71], v182 offset:0x1100
	ds_read_b64_tr_b16 v[72:73], v182 offset:0x2000
	ds_read_b64_tr_b16 v[74:75], v182 offset:0x2100
	ds_read_b64_tr_b16 v[76:77], v182 offset:0x3000
	ds_read_b64_tr_b16 v[78:79], v182 offset:0x3100
	s_waitcnt lgkmcnt(0)
	v_mfma_f32_32x32x16_bf16 v[48:63], v[64:67], v[96:99], v[48:63]
	v_max_f32_e32 v64, v128, v129
	v_max3_f32 v64, v64, v130, v131
	v_max3_f32 v64, v64, v132, v133
	v_max3_f32 v64, v64, v134, v135
	v_max3_f32 v64, v64, v136, v137
	v_mfma_f32_32x32x16_bf16 v[48:63], v[68:71], v[108:111], v[48:63]
	v_max3_f32 v64, v64, v138, v139
	v_max3_f32 v66, v64, v140, v141
	ds_read_b64_tr_b16 v[64:65], v182 offset:0x200
	v_max3_f32 v180, v66, v142, v143
	ds_read_b64_tr_b16 v[66:67], v182 offset:0x300
	ds_read_b64_tr_b16 v[68:69], v182 offset:0x1200
	ds_read_b64_tr_b16 v[70:71], v182 offset:0x1300
	v_mfma_f32_32x32x16_bf16 v[48:63], v[72:75], v[100:103], v[48:63]
	ds_read_b64_tr_b16 v[72:73], v182 offset:0x2200
	ds_read_b64_tr_b16 v[74:75], v182 offset:0x2300
	ds_read_b64_tr_b16 v[218:219], v182 offset:0x3200
	ds_read_b64_tr_b16 v[220:221], v182 offset:0x3300
	v_mfma_f32_32x32x16_bf16 v[48:63], v[76:79], v[104:107], v[48:63]
	s_waitcnt lgkmcnt(0)
	v_mfma_f32_32x32x16_bf16 v[32:47], v[64:67], v[96:99], v[32:47]
	v_max3_f32 v76, v180, v112, v113
	v_max3_f32 v64, v76, v114, v115
	ds_read_b64_tr_b16 v[66:67], v182 offset:0x400
	v_max3_f32 v64, v64, v116, v117
	v_max3_f32 v64, v64, v118, v119
	v_max3_f32 v64, v64, v120, v121
	v_max3_f32 v64, v64, v122, v123
	v_mfma_f32_32x32x16_bf16 v[32:47], v[68:71], v[108:111], v[32:47]
	ds_read_b64_tr_b16 v[68:69], v182 offset:0x500
	ds_read_b64_tr_b16 v[70:71], v182 offset:0x1400
	v_max3_f32 v64, v64, v124, v125
	v_max3_f32 v64, v64, v126, v127
	v_mfma_f32_32x32x16_bf16 v[32:47], v[72:75], v[100:103], v[32:47]
	ds_read_b64_tr_b16 v[72:73], v182 offset:0x1500
	ds_read_b64_tr_b16 v[74:75], v182 offset:0x2400
	ds_read_b64_tr_b16 v[76:77], v182 offset:0x2500
	ds_read_b64_tr_b16 v[222:223], v182 offset:0x3400
	ds_read_b64_tr_b16 v[224:225], v182 offset:0x3500
	v_mfma_f32_32x32x16_bf16 v[32:47], v[218:221], v[104:107], v[32:47]
	s_waitcnt lgkmcnt(0)
	v_mfma_f32_32x32x16_bf16 v[16:31], v[66:69], v[96:99], v[16:31]
	v_cmp_ge_f32_e32 vcc, s26, v64
	s_cmp_eq_u64 vcc, exec
	v_mfma_f32_32x32x16_bf16 v[16:31], v[70:73], v[108:111], v[16:31]
	v_mfma_f32_32x32x16_bf16 v[16:31], v[74:77], v[100:103], v[16:31]
	v_mfma_f32_32x32x16_bf16 v[16:31], v[222:225], v[104:107], v[16:31]
	s_cbranch_scc0 .LBB4_810
	v_mov_b32_e32 v180, 1.0

; #define AT_SBAR() __builtin_amdgcn_sched_barrier(0)
; template <int OFF> DI s16x4 tr_read(int vb) { s16x4 r; asm volatile("ds_read_b64_tr_b16 %0, %1 offset:%2" : "=&v"(r) : "v"(vb), "i"(OFF) : "memory"); return r; }
; template <int D0> DI void pv_one(f32x16& od, int vb, bf16x8 pa0, bf16x8 pa1, bf16x8 pa2, bf16x8 pa3) {
;     const s16x4 l0 = tr_read<v_rd_off(D0, 0, 0)>(vb), h0 = tr_read<v_rd_off(D0, 0, 1)>(vb), l1 = tr_read<v_rd_off(D0, 1, 0)>(vb), h1 = tr_read<v_rd_off(D0, 1, 1)>(vb);
;     const s16x4 l2 = tr_read<v_rd_off(D0, 2, 0)>(vb), h2 = tr_read<v_rd_off(D0, 2, 1)>(vb), l3 = tr_read<v_rd_off(D0, 3, 0)>(vb), h3 = tr_read<v_rd_off(D0, 3, 1)>(vb);
;     asm volatile("s_waitcnt lgkmcnt(0)" ::: "memory"); AT_SBAR();
;     ...
;     od = __builtin_amdgcn_mfma_f32_32x32x16_bf16(AT_PK(l0, h0), pa0, od, 0, 0, 0);
;     od = __builtin_amdgcn_mfma_f32_32x32x16_bf16(AT_PK(l1, h1), pa1, od, 0, 0, 0);
;     od = __builtin_amdgcn_mfma_f32_32x32x16_bf16(AT_PK(l2, h2), pa2, od, 0, 0, 0);
;     od = __builtin_amdgcn_mfma_f32_32x32x16_bf16(AT_PK(l3, h3), pa3, od, 0, 0, 0);
;     ...
; }
; DI void pv_all_sm(f32x16* o, int vb, bf16x8 pa0, bf16x8 pa1, bf16x8 pa2, bf16x8 pa3, f32x16& p0, f32x16& p1, float& m_ref, f32x16& negm, float& alpha) {
;     pv_one<0>(o[0], vb, pa0, pa1, pa2, pa3);
;     float pmax = p0[0];
; #pragma unroll
;     for (int r = 1; r < 16; ++r) pmax = fmaxf(pmax, p0[r]);
;     pv_one<1>(o[1], vb, pa0, pa1, pa2, pa3);
; #pragma unroll
;     for (int r = 0; r < 16; ++r) pmax = fmaxf(pmax, p1[r]);
;     { auto rr = __builtin_amdgcn_permlane32_swap(__float_as_uint(pmax), __float_as_uint(pmax), false, false); pmax = fmaxf(__uint_as_float(rr[0]), __uint_as_float(rr[1])); }
;     pv_one<2>(o[2], vb, pa0, pa1, pa2, pa3);
;     alpha = 1.f;
;     if (__builtin_expect(!__all(pmax <= THRL), 0)) {
;         const float dl = fmaxf(pmax, 0.f); m_ref += dl; alpha = __builtin_amdgcn_exp2f(-dl);
; #pragma unroll
;         for (int r = 0; r < 16; ++r) { p0[r] -= dl; p1[r] -= dl; }
; #pragma unroll
;         for (int r = 0; r < 16; ++r) negm[r] = -m_ref;
;     }
.LBB4_798:
	v_lshl_add_u32 v219, s30, 14, v253
	ds_read_b64_tr_b16 v[220:221], v219 offset:0
	ds_read_b64_tr_b16 v[222:223], v219 offset:0x100
	ds_read_b64_tr_b16 v[224:225], v219 offset:0x1000
	ds_read_b64_tr_b16 v[226:227], v219 offset:0x1100
	ds_read_b64_tr_b16 v[228:229], v219 offset:0x2000
	ds_read_b64_tr_b16 v[230:231], v219 offset:0x2100
	ds_read_b64_tr_b16 v[232:233], v219 offset:0x3000
	ds_read_b64_tr_b16 v[234:235], v219 offset:0x3100
	s_waitcnt lgkmcnt(0)
	v_mfma_f32_32x32x16_bf16 v[48:63], v[220:223], v[120:123], v[48:63]
	v_max_f32_e32 v182, v128, v129
	ds_read_b64_tr_b16 v[220:221], v219 offset:0x200
	ds_read_b64_tr_b16 v[222:223], v219 offset:0x300
	v_max3_f32 v182, v182, v130, v131
	v_max3_f32 v182, v182, v132, v133
	v_mfma_f32_32x32x16_bf16 v[48:63], v[224:227], v[124:127], v[48:63]
	ds_read_b64_tr_b16 v[224:225], v219 offset:0x1200
	ds_read_b64_tr_b16 v[226:227], v219 offset:0x1300
	v_max3_f32 v182, v182, v134, v135
	v_max3_f32 v182, v182, v136, v137
	v_max3_f32 v182, v182, v138, v139
	v_max3_f32 v182, v182, v140, v141
	v_max3_f32 v182, v182, v142, v143
	v_mfma_f32_32x32x16_bf16 v[48:63], v[228:231], v[112:115], v[48:63]
	ds_read_b64_tr_b16 v[228:229], v219 offset:0x2200
	ds_read_b64_tr_b16 v[230:231], v219 offset:0x2300
	ds_read_b64_tr_b16 v[236:237], v219 offset:0x3200
	ds_read_b64_tr_b16 v[238:239], v219 offset:0x3300
	v_mfma_f32_32x32x16_bf16 v[48:63], v[232:235], v[116:119], v[48:63]
	s_waitcnt lgkmcnt(0)
	v_mfma_f32_32x32x16_bf16 v[32:47], v[220:223], v[120:123], v[32:47]
	v_max3_f32 v182, v182, v96, v97
	v_max3_f32 v182, v182, v98, v99
	ds_read_b64_tr_b16 v[222:223], v219 offset:0x400
	v_max3_f32 v182, v182, v100, v101
	v_max3_f32 v182, v182, v102, v103
	v_max3_f32 v182, v182, v104, v105
	v_max3_f32 v182, v182, v106, v107
	v_mfma_f32_32x32x16_bf16 v[32:47], v[224:227], v[124:127], v[32:47]
	ds_read_b64_tr_b16 v[224:225], v219 offset:0x500
	ds_read_b64_tr_b16 v[226:227], v219 offset:0x1400
	v_max3_f32 v182, v182, v108, v109
	v_max3_f32 v182, v182, v110, v111
	v_mov_b32_e32 v220, v182
	v_mfma_f32_32x32x16_bf16 v[32:47], v[228:231], v[112:115], v[32:47]
	ds_read_b64_tr_b16 v[228:229], v219 offset:0x1500
	ds_read_b64_tr_b16 v[230:231], v219 offset:0x2400
	ds_read_b64_tr_b16 v[232:233], v219 offset:0x2500
	ds_read_b64_tr_b16 v[240:241], v219 offset:0x3400
	ds_read_b64_tr_b16 v[242:243], v219 offset:0x3500
	v_mfma_f32_32x32x16_bf16 v[32:47], v[236:239], v[116:119], v[32:47]
	s_waitcnt lgkmcnt(0)
	v_mfma_f32_32x32x16_bf16 v[16:31], v[222:225], v[120:123], v[16:31]
	v_cmp_ge_f32_e32 vcc, s26, v220
	s_cmp_eq_u64 vcc, exec
	v_mov_b32_e32 v182, 1.0
	v_mfma_f32_32x32x16_bf16 v[16:31], v[226:229], v[124:127], v[16:31]
	v_mfma_f32_32x32x16_bf16 v[16:31], v[230:233], v[112:115], v[16:31]
	v_mfma_f32_32x32x16_bf16 v[16:31], v[240:243], v[116:119], v[16:31]
	s_cbranch_scc0 .LBB4_811

; DI void pv_all_sm(f32x16* o, int vb, bf16x8 pa0, bf16x8 pa1, bf16x8 pa2, bf16x8 pa3, f32x16& p0, f32x16& p1, float& m_ref, f32x16& negm, float& alpha) {
;     ...
;     { auto rr = __builtin_amdgcn_permlane32_swap(__float_as_uint(pmax), __float_as_uint(pmax), false, false); pmax = fmaxf(__uint_as_float(rr[0]), __uint_as_float(rr[1])); }
;     pv_one<2>(o[2], vb, pa0, pa1, pa2, pa3);
;     alpha = 1.f;
;     if (__builtin_expect(!__all(pmax <= THRL), 0)) {
;         const float dl = fmaxf(pmax, 0.f); m_ref += dl; alpha = __builtin_amdgcn_exp2f(-dl);
; #pragma unroll
;         for (int r = 0; r < 16; ++r) { p0[r] -= dl; p1[r] -= dl; }
; #pragma unroll
;         for (int r = 0; r < 16; ++r) negm[r] = -m_ref;
;     }
.LBB4_810:
	v_mov_b32_e32 v65, v64
	s_nop 1
	v_permlane32_swap_b32_e32 v64, v65
	v_max_f32_e32 v64, v64, v65
	v_max_f32_e32 v64, v64, v64
	v_max_f32_e32 v64, 0, v64
	v_exp_f32_e64 v180, -v64
	v_add_f32_e32 v212, v212, v64
	v_pk_add_f32 v[128:129], v[128:129], v[64:65] op_sel_hi:[1,0] neg_lo:[0,1] neg_hi:[0,1]
	v_pk_add_f32 v[130:131], v[130:131], v[64:65] op_sel_hi:[1,0] neg_lo:[0,1] neg_hi:[0,1]
	v_pk_add_f32 v[132:133], v[132:133], v[64:65] op_sel_hi:[1,0] neg_lo:[0,1] neg_hi:[0,1]
	v_pk_add_f32 v[134:135], v[134:135], v[64:65] op_sel_hi:[1,0] neg_lo:[0,1] neg_hi:[0,1]
	v_pk_add_f32 v[136:137], v[136:137], v[64:65] op_sel_hi:[1,0] neg_lo:[0,1] neg_hi:[0,1]
	v_pk_add_f32 v[138:139], v[138:139], v[64:65] op_sel_hi:[1,0] neg_lo:[0,1] neg_hi:[0,1]
	v_pk_add_f32 v[140:141], v[140:141], v[64:65] op_sel_hi:[1,0] neg_lo:[0,1] neg_hi:[0,1]
	v_pk_add_f32 v[142:143], v[142:143], v[64:65] op_sel_hi:[1,0] neg_lo:[0,1] neg_hi:[0,1]
	v_sub_f32_e32 v127, v127, v64
	v_sub_f32_e32 v126, v126, v64
	v_sub_f32_e32 v125, v125, v64
	v_sub_f32_e32 v124, v124, v64
	v_sub_f32_e32 v123, v123, v64
	v_sub_f32_e32 v122, v122, v64
	v_sub_f32_e32 v121, v121, v64
	v_sub_f32_e32 v120, v120, v64
	v_sub_f32_e32 v119, v119, v64
	v_sub_f32_e32 v118, v118, v64
	v_sub_f32_e32 v117, v117, v64
	v_sub_f32_e32 v116, v116, v64
	v_sub_f32_e32 v115, v115, v64
	v_sub_f32_e32 v114, v114, v64
	v_sub_f32_e32 v113, v113, v64
	v_sub_f32_e32 v112, v112, v64
	v_xor_b32_e32 v64, 0x80000000, v212
	v_mov_b32_e32 v65, v64
	v_mov_b32_e32 v66, v64
	v_mov_b32_e32 v67, v64
	v_mov_b32_e32 v68, v64
	v_mov_b32_e32 v69, v64
	v_mov_b32_e32 v70, v64
	v_mov_b32_e32 v71, v64
	v_mov_b32_e32 v72, v64
	v_mov_b32_e32 v73, v64
	v_mov_b32_e32 v74, v64
	v_mov_b32_e32 v75, v64
	v_mov_b32_e32 v76, v64
	v_mov_b32_e32 v77, v64
	v_mov_b32_e32 v78, v64
	v_mov_b32_e32 v79, v64
	v_mov_b32_e32 v80, v64
	v_mov_b32_e32 v81, v64
	v_mov_b32_e32 v82, v64
	v_mov_b32_e32 v83, v64
	v_mov_b32_e32 v84, v64
	v_mov_b32_e32 v85, v64
	v_mov_b32_e32 v86, v64
	v_mov_b32_e32 v87, v64
	v_mov_b32_e32 v88, v64
	v_mov_b32_e32 v89, v64
	v_mov_b32_e32 v90, v64
	v_mov_b32_e32 v91, v64
	v_mov_b32_e32 v92, v64
	v_mov_b32_e32 v93, v64
	v_mov_b32_e32 v94, v64
	v_mov_b32_e32 v95, v64
	s_branch .LBB4_779
.LBB4_811:
	v_mov_b32_e32 v254, v220
	s_nop 1
	v_permlane32_swap_b32_e32 v220, v254
	v_max_f32_e32 v220, v220, v254
	v_max_f32_e32 v64, v220, v220
	v_max_f32_e32 v64, 0, v64
	v_exp_f32_e64 v182, -v64
	v_add_f32_e32 v212, v212, v64
	v_pk_add_f32 v[128:129], v[128:129], v[64:65] op_sel_hi:[1,0] neg_lo:[0,1] neg_hi:[0,1]
	v_pk_add_f32 v[130:131], v[130:131], v[64:65] op_sel_hi:[1,0] neg_lo:[0,1] neg_hi:[0,1]
	v_pk_add_f32 v[132:133], v[132:133], v[64:65] op_sel_hi:[1,0] neg_lo:[0,1] neg_hi:[0,1]
	v_pk_add_f32 v[134:135], v[134:135], v[64:65] op_sel_hi:[1,0] neg_lo:[0,1] neg_hi:[0,1]
	v_pk_add_f32 v[136:137], v[136:137], v[64:65] op_sel_hi:[1,0] neg_lo:[0,1] neg_hi:[0,1]
	v_pk_add_f32 v[138:139], v[138:139], v[64:65] op_sel_hi:[1,0] neg_lo:[0,1] neg_hi:[0,1]
	v_pk_add_f32 v[140:141], v[140:141], v[64:65] op_sel_hi:[1,0] neg_lo:[0,1] neg_hi:[0,1]
	v_pk_add_f32 v[142:143], v[142:143], v[64:65] op_sel_hi:[1,0] neg_lo:[0,1] neg_hi:[0,1]
	v_sub_f32_e32 v111, v111, v64
	v_sub_f32_e32 v110, v110, v64
	v_sub_f32_e32 v109, v109, v64
	v_sub_f32_e32 v108, v108, v64
	v_sub_f32_e32 v107, v107, v64
	v_sub_f32_e32 v106, v106, v64
	v_sub_f32_e32 v105, v105, v64
	v_sub_f32_e32 v104, v104, v64
	v_sub_f32_e32 v103, v103, v64
	v_sub_f32_e32 v102, v102, v64
	v_sub_f32_e32 v101, v101, v64
	v_sub_f32_e32 v100, v100, v64
	v_sub_f32_e32 v99, v99, v64
	v_sub_f32_e32 v98, v98, v64
	v_sub_f32_e32 v97, v97, v64
	v_sub_f32_e32 v96, v96, v64
	v_xor_b32_e32 v64, 0x80000000, v212
	v_mov_b32_e32 v65, v64
	v_mov_b32_e32 v66, v64
	v_mov_b32_e32 v67, v64
	v_mov_b32_e32 v68, v64
	v_mov_b32_e32 v69, v64
	v_mov_b32_e32 v70, v64
	v_mov_b32_e32 v71, v64
	v_mov_b32_e32 v72, v64
	v_mov_b32_e32 v73, v64
	v_mov_b32_e32 v74, v64
	v_mov_b32_e32 v75, v64
	v_mov_b32_e32 v76, v64
	v_mov_b32_e32 v77, v64
	v_mov_b32_e32 v78, v64
	v_mov_b32_e32 v79, v64
	v_mov_b32_e32 v80, v64
	v_mov_b32_e32 v81, v64
	v_mov_b32_e32 v82, v64
	v_mov_b32_e32 v83, v64
	v_mov_b32_e32 v84, v64
	v_mov_b32_e32 v85, v64
	v_mov_b32_e32 v86, v64
	v_mov_b32_e32 v87, v64
	v_mov_b32_e32 v88, v64
	v_mov_b32_e32 v89, v64
	v_mov_b32_e32 v90, v64
	v_mov_b32_e32 v91, v64
	v_mov_b32_e32 v92, v64
	v_mov_b32_e32 v93, v64
	v_mov_b32_e32 v94, v64
	v_mov_b32_e32 v95, v64
	s_branch .LBB4_799

; #define AT_SBAR() __builtin_amdgcn_sched_barrier(0)
; template <int OFF> DI s16x4 tr_read(int vb) { s16x4 r; asm volatile("ds_read_b64_tr_b16 %0, %1 offset:%2" : "=&v"(r) : "v"(vb), "i"(OFF) : "memory"); return r; }
; template <int D0> DI void pv_one(f32x16& od, int vb, bf16x8 pa0, bf16x8 pa1, bf16x8 pa2, bf16x8 pa3) {
;     const s16x4 l0 = tr_read<v_rd_off(D0, 0, 0)>(vb), h0 = tr_read<v_rd_off(D0, 0, 1)>(vb), l1 = tr_read<v_rd_off(D0, 1, 0)>(vb), h1 = tr_read<v_rd_off(D0, 1, 1)>(vb);
;     const s16x4 l2 = tr_read<v_rd_off(D0, 2, 0)>(vb), h2 = tr_read<v_rd_off(D0, 2, 1)>(vb), l3 = tr_read<v_rd_off(D0, 3, 0)>(vb), h3 = tr_read<v_rd_off(D0, 3, 1)>(vb);
;     asm volatile("s_waitcnt lgkmcnt(0)" ::: "memory"); AT_SBAR();
;     ...
;     od = __builtin_amdgcn_mfma_f32_32x32x16_bf16(AT_PK(l0, h0), pa0, od, 0, 0, 0);
;     od = __builtin_amdgcn_mfma_f32_32x32x16_bf16(AT_PK(l1, h1), pa1, od, 0, 0, 0);
;     od = __builtin_amdgcn_mfma_f32_32x32x16_bf16(AT_PK(l2, h2), pa2, od, 0, 0, 0);
;     od = __builtin_amdgcn_mfma_f32_32x32x16_bf16(AT_PK(l3, h3), pa3, od, 0, 0, 0);
;     ...
; }
; DI void pv_all_sm(f32x16* o, int vb, bf16x8 pa0, bf16x8 pa1, bf16x8 pa2, bf16x8 pa3, f32x16& p0, f32x16& p1, float& m_ref, f32x16& negm, float& alpha) {
;     pv_one<0>(o[0], vb, pa0, pa1, pa2, pa3);
;     float pmax = p0[0];
; #pragma unroll
;     for (int r = 1; r < 16; ++r) pmax = fmaxf(pmax, p0[r]);
;     pv_one<1>(o[1], vb, pa0, pa1, pa2, pa3);
; #pragma unroll
;     for (int r = 0; r < 16; ++r) pmax = fmaxf(pmax, p1[r]);
;     { auto rr = __builtin_amdgcn_permlane32_swap(__float_as_uint(pmax), __float_as_uint(pmax), false, false); pmax = fmaxf(__uint_as_float(rr[0]), __uint_as_float(rr[1])); }
;     pv_one<2>(o[2], vb, pa0, pa1, pa2, pa3);
;     alpha = 1.f;
;     if (__builtin_expect(!__all(pmax <= THRL), 0)) {
;         const float dl = fmaxf(pmax, 0.f); m_ref += dl; alpha = __builtin_amdgcn_exp2f(-dl);
; #pragma unroll
;         for (int r = 0; r < 16; ++r) { p0[r] -= dl; p1[r] -= dl; }
; #pragma unroll
;         for (int r = 0; r < 16; ++r) negm[r] = -m_ref;
;     }
.LBB4_851:
	s_lshl_b32 s65, s63, 14
	v_add_u32_e32 v182, s65, v253
	ds_read_b64_tr_b16 v[64:65], v182 offset:0
	ds_read_b64_tr_b16 v[66:67], v182 offset:0x100
	ds_read_b64_tr_b16 v[68:69], v182 offset:0x1000
	ds_read_b64_tr_b16 v[70:71], v182 offset:0x1100
	ds_read_b64_tr_b16 v[72:73], v182 offset:0x2000
	ds_read_b64_tr_b16 v[74:75], v182 offset:0x2100
	ds_read_b64_tr_b16 v[76:77], v182 offset:0x3000
	ds_read_b64_tr_b16 v[78:79], v182 offset:0x3100
	s_waitcnt lgkmcnt(0)
	v_mfma_f32_32x32x16_bf16 v[32:47], v[64:67], v[96:99], v[32:47]
	v_max_f32_e32 v64, v128, v129
	v_max3_f32 v64, v64, v130, v131
	v_max3_f32 v64, v64, v132, v133
	v_max3_f32 v64, v64, v134, v135
	v_max3_f32 v64, v64, v136, v137
	v_mfma_f32_32x32x16_bf16 v[32:47], v[68:71], v[108:111], v[32:47]
	v_max3_f32 v64, v64, v138, v139
	v_max3_f32 v66, v64, v140, v141
	ds_read_b64_tr_b16 v[64:65], v182 offset:0x200
	v_max3_f32 v180, v66, v142, v143
	ds_read_b64_tr_b16 v[66:67], v182 offset:0x300
	ds_read_b64_tr_b16 v[68:69], v182 offset:0x1200
	ds_read_b64_tr_b16 v[70:71], v182 offset:0x1300
	v_mfma_f32_32x32x16_bf16 v[32:47], v[72:75], v[100:103], v[32:47]
	ds_read_b64_tr_b16 v[72:73], v182 offset:0x2200
	ds_read_b64_tr_b16 v[74:75], v182 offset:0x2300
	ds_read_b64_tr_b16 v[214:215], v182 offset:0x3200
	ds_read_b64_tr_b16 v[216:217], v182 offset:0x3300
	v_mfma_f32_32x32x16_bf16 v[32:47], v[76:79], v[104:107], v[32:47]
	s_waitcnt lgkmcnt(0)
	v_mfma_f32_32x32x16_bf16 v[48:63], v[64:67], v[96:99], v[48:63]
	v_max3_f32 v76, v180, v112, v113
	v_max3_f32 v64, v76, v114, v115
	ds_read_b64_tr_b16 v[66:67], v182 offset:0x400
	v_max3_f32 v64, v64, v116, v117
	v_max3_f32 v64, v64, v118, v119
	v_max3_f32 v64, v64, v120, v121
	v_max3_f32 v64, v64, v122, v123
	v_mfma_f32_32x32x16_bf16 v[48:63], v[68:71], v[108:111], v[48:63]
	ds_read_b64_tr_b16 v[68:69], v182 offset:0x500
	ds_read_b64_tr_b16 v[70:71], v182 offset:0x1400
	v_max3_f32 v64, v64, v124, v125
	v_max3_f32 v64, v64, v126, v127
	v_mfma_f32_32x32x16_bf16 v[48:63], v[72:75], v[100:103], v[48:63]
	ds_read_b64_tr_b16 v[72:73], v182 offset:0x1500
	ds_read_b64_tr_b16 v[74:75], v182 offset:0x2400
	ds_read_b64_tr_b16 v[76:77], v182 offset:0x2500
	ds_read_b64_tr_b16 v[218:219], v182 offset:0x3400
	ds_read_b64_tr_b16 v[220:221], v182 offset:0x3500
	v_mfma_f32_32x32x16_bf16 v[48:63], v[214:217], v[104:107], v[48:63]
	s_waitcnt lgkmcnt(0)
	v_mfma_f32_32x32x16_bf16 v[16:31], v[66:69], v[96:99], v[16:31]
	v_cmp_ge_f32_e32 vcc, s15, v64
	s_cmp_eq_u64 vcc, exec
	v_mfma_f32_32x32x16_bf16 v[16:31], v[70:73], v[108:111], v[16:31]
	v_mfma_f32_32x32x16_bf16 v[16:31], v[74:77], v[100:103], v[16:31]
	v_mfma_f32_32x32x16_bf16 v[16:31], v[218:221], v[104:107], v[16:31]
	s_cbranch_scc0 .LBB4_884
	v_mov_b32_e32 v180, 1.0

; #define AT_SBAR() __builtin_amdgcn_sched_barrier(0)
; template <int OFF> DI s16x4 tr_read(int vb) { s16x4 r; asm volatile("ds_read_b64_tr_b16 %0, %1 offset:%2" : "=&v"(r) : "v"(vb), "i"(OFF) : "memory"); return r; }
; template <int D0> DI void pv_one(f32x16& od, int vb, bf16x8 pa0, bf16x8 pa1, bf16x8 pa2, bf16x8 pa3) {
;     const s16x4 l0 = tr_read<v_rd_off(D0, 0, 0)>(vb), h0 = tr_read<v_rd_off(D0, 0, 1)>(vb), l1 = tr_read<v_rd_off(D0, 1, 0)>(vb), h1 = tr_read<v_rd_off(D0, 1, 1)>(vb);
;     const s16x4 l2 = tr_read<v_rd_off(D0, 2, 0)>(vb), h2 = tr_read<v_rd_off(D0, 2, 1)>(vb), l3 = tr_read<v_rd_off(D0, 3, 0)>(vb), h3 = tr_read<v_rd_off(D0, 3, 1)>(vb);
;     asm volatile("s_waitcnt lgkmcnt(0)" ::: "memory"); AT_SBAR();
;     ...
;     od = __builtin_amdgcn_mfma_f32_32x32x16_bf16(AT_PK(l0, h0), pa0, od, 0, 0, 0);
;     od = __builtin_amdgcn_mfma_f32_32x32x16_bf16(AT_PK(l1, h1), pa1, od, 0, 0, 0);
;     od = __builtin_amdgcn_mfma_f32_32x32x16_bf16(AT_PK(l2, h2), pa2, od, 0, 0, 0);
;     od = __builtin_amdgcn_mfma_f32_32x32x16_bf16(AT_PK(l3, h3), pa3, od, 0, 0, 0);
;     ...
; }
; DI void pv_all_sm(f32x16* o, int vb, bf16x8 pa0, bf16x8 pa1, bf16x8 pa2, bf16x8 pa3, f32x16& p0, f32x16& p1, float& m_ref, f32x16& negm, float& alpha) {
;     pv_one<0>(o[0], vb, pa0, pa1, pa2, pa3);
;     float pmax = p0[0];
; #pragma unroll
;     for (int r = 1; r < 16; ++r) pmax = fmaxf(pmax, p0[r]);
;     pv_one<1>(o[1], vb, pa0, pa1, pa2, pa3);
; #pragma unroll
;     for (int r = 0; r < 16; ++r) pmax = fmaxf(pmax, p1[r]);
;     { auto rr = __builtin_amdgcn_permlane32_swap(__float_as_uint(pmax), __float_as_uint(pmax), false, false); pmax = fmaxf(__uint_as_float(rr[0]), __uint_as_float(rr[1])); }
;     pv_one<2>(o[2], vb, pa0, pa1, pa2, pa3);
;     alpha = 1.f;
;     if (__builtin_expect(!__all(pmax <= THRL), 0)) {
;         const float dl = fmaxf(pmax, 0.f); m_ref += dl; alpha = __builtin_amdgcn_exp2f(-dl);
; #pragma unroll
;         for (int r = 0; r < 16; ++r) { p0[r] -= dl; p1[r] -= dl; }
; #pragma unroll
;         for (int r = 0; r < 16; ++r) negm[r] = -m_ref;
;     }
.LBB4_872:
	v_lshl_add_u32 v215, s64, 14, v253
	ds_read_b64_tr_b16 v[216:217], v215 offset:0
	ds_read_b64_tr_b16 v[218:219], v215 offset:0x100
	ds_read_b64_tr_b16 v[220:221], v215 offset:0x1000
	ds_read_b64_tr_b16 v[222:223], v215 offset:0x1100
	ds_read_b64_tr_b16 v[224:225], v215 offset:0x2000
	ds_read_b64_tr_b16 v[226:227], v215 offset:0x2100
	ds_read_b64_tr_b16 v[228:229], v215 offset:0x3000
	ds_read_b64_tr_b16 v[230:231], v215 offset:0x3100
	s_waitcnt lgkmcnt(0)
	v_mfma_f32_32x32x16_bf16 v[32:47], v[216:219], v[120:123], v[32:47]
	v_max_f32_e32 v182, v128, v129
	ds_read_b64_tr_b16 v[216:217], v215 offset:0x200
	ds_read_b64_tr_b16 v[218:219], v215 offset:0x300
	v_max3_f32 v182, v182, v130, v131
	v_max3_f32 v182, v182, v132, v133
	v_mfma_f32_32x32x16_bf16 v[32:47], v[220:223], v[124:127], v[32:47]
	ds_read_b64_tr_b16 v[220:221], v215 offset:0x1200
	ds_read_b64_tr_b16 v[222:223], v215 offset:0x1300
	v_max3_f32 v182, v182, v134, v135
	v_max3_f32 v182, v182, v136, v137
	v_max3_f32 v182, v182, v138, v139
	v_max3_f32 v182, v182, v140, v141
	v_max3_f32 v182, v182, v142, v143
	v_mfma_f32_32x32x16_bf16 v[32:47], v[224:227], v[112:115], v[32:47]
	ds_read_b64_tr_b16 v[224:225], v215 offset:0x2200
	ds_read_b64_tr_b16 v[226:227], v215 offset:0x2300
	ds_read_b64_tr_b16 v[232:233], v215 offset:0x3200
	ds_read_b64_tr_b16 v[234:235], v215 offset:0x3300
	v_mfma_f32_32x32x16_bf16 v[32:47], v[228:231], v[116:119], v[32:47]
	s_waitcnt lgkmcnt(0)
	v_mfma_f32_32x32x16_bf16 v[48:63], v[216:219], v[120:123], v[48:63]
	v_max3_f32 v182, v182, v96, v97
	v_max3_f32 v182, v182, v98, v99
	ds_read_b64_tr_b16 v[218:219], v215 offset:0x400
	v_max3_f32 v182, v182, v100, v101
	v_max3_f32 v182, v182, v102, v103
	v_max3_f32 v182, v182, v104, v105
	v_max3_f32 v182, v182, v106, v107
	v_mfma_f32_32x32x16_bf16 v[48:63], v[220:223], v[124:127], v[48:63]
	ds_read_b64_tr_b16 v[220:221], v215 offset:0x500
	ds_read_b64_tr_b16 v[222:223], v215 offset:0x1400
	v_max3_f32 v182, v182, v108, v109
	v_max3_f32 v182, v182, v110, v111
	v_mov_b32_e32 v216, v182
	v_mfma_f32_32x32x16_bf16 v[48:63], v[224:227], v[112:115], v[48:63]
	ds_read_b64_tr_b16 v[224:225], v215 offset:0x1500
	ds_read_b64_tr_b16 v[226:227], v215 offset:0x2400
	ds_read_b64_tr_b16 v[228:229], v215 offset:0x2500
	ds_read_b64_tr_b16 v[236:237], v215 offset:0x3400
	ds_read_b64_tr_b16 v[238:239], v215 offset:0x3500
	v_mfma_f32_32x32x16_bf16 v[48:63], v[232:235], v[116:119], v[48:63]
	s_waitcnt lgkmcnt(0)
	v_mfma_f32_32x32x16_bf16 v[16:31], v[218:221], v[120:123], v[16:31]
	v_cmp_ge_f32_e32 vcc, s15, v216
	s_cmp_eq_u64 vcc, exec
	v_mov_b32_e32 v182, 1.0
	v_mfma_f32_32x32x16_bf16 v[16:31], v[222:225], v[124:127], v[16:31]
	v_mfma_f32_32x32x16_bf16 v[16:31], v[226:229], v[112:115], v[16:31]
	v_mfma_f32_32x32x16_bf16 v[16:31], v[236:239], v[116:119], v[16:31]
	s_cbranch_scc0 .LBB4_885

; DI void pv_all_sm(f32x16* o, int vb, bf16x8 pa0, bf16x8 pa1, bf16x8 pa2, bf16x8 pa3, f32x16& p0, f32x16& p1, float& m_ref, f32x16& negm, float& alpha) {
;     ...
;     { auto rr = __builtin_amdgcn_permlane32_swap(__float_as_uint(pmax), __float_as_uint(pmax), false, false); pmax = fmaxf(__uint_as_float(rr[0]), __uint_as_float(rr[1])); }
;     pv_one<2>(o[2], vb, pa0, pa1, pa2, pa3);
;     alpha = 1.f;
;     if (__builtin_expect(!__all(pmax <= THRL), 0)) {
;         const float dl = fmaxf(pmax, 0.f); m_ref += dl; alpha = __builtin_amdgcn_exp2f(-dl);
; #pragma unroll
;         for (int r = 0; r < 16; ++r) { p0[r] -= dl; p1[r] -= dl; }
; #pragma unroll
;         for (int r = 0; r < 16; ++r) negm[r] = -m_ref;
;     }
.LBB4_885:
	v_mov_b32_e32 v254, v216
	s_nop 1
	v_permlane32_swap_b32_e32 v216, v254
	v_max_f32_e32 v216, v216, v254
	v_max_f32_e32 v64, v216, v216
	v_max_f32_e32 v64, 0, v64
	v_exp_f32_e64 v182, -v64
	v_add_f32_e32 v208, v208, v64
	v_pk_add_f32 v[128:129], v[128:129], v[64:65] op_sel_hi:[1,0] neg_lo:[0,1] neg_hi:[0,1]
	v_pk_add_f32 v[130:131], v[130:131], v[64:65] op_sel_hi:[1,0] neg_lo:[0,1] neg_hi:[0,1]
	v_pk_add_f32 v[132:133], v[132:133], v[64:65] op_sel_hi:[1,0] neg_lo:[0,1] neg_hi:[0,1]
	v_pk_add_f32 v[134:135], v[134:135], v[64:65] op_sel_hi:[1,0] neg_lo:[0,1] neg_hi:[0,1]
	v_pk_add_f32 v[136:137], v[136:137], v[64:65] op_sel_hi:[1,0] neg_lo:[0,1] neg_hi:[0,1]
	v_pk_add_f32 v[138:139], v[138:139], v[64:65] op_sel_hi:[1,0] neg_lo:[0,1] neg_hi:[0,1]
	v_pk_add_f32 v[140:141], v[140:141], v[64:65] op_sel_hi:[1,0] neg_lo:[0,1] neg_hi:[0,1]
	v_pk_add_f32 v[142:143], v[142:143], v[64:65] op_sel_hi:[1,0] neg_lo:[0,1] neg_hi:[0,1]
	v_sub_f32_e32 v111, v111, v64
	v_sub_f32_e32 v110, v110, v64
	v_sub_f32_e32 v109, v109, v64
	v_sub_f32_e32 v108, v108, v64
	v_sub_f32_e32 v107, v107, v64
	v_sub_f32_e32 v106, v106, v64
	v_sub_f32_e32 v105, v105, v64
	v_sub_f32_e32 v104, v104, v64
	v_sub_f32_e32 v103, v103, v64
	v_sub_f32_e32 v102, v102, v64
	v_sub_f32_e32 v101, v101, v64
	v_sub_f32_e32 v100, v100, v64
	v_sub_f32_e32 v99, v99, v64
	v_sub_f32_e32 v98, v98, v64
	v_sub_f32_e32 v97, v97, v64
	v_sub_f32_e32 v96, v96, v64
	v_xor_b32_e32 v64, 0x80000000, v208
	v_mov_b32_e32 v65, v64
	v_mov_b32_e32 v66, v64
	v_mov_b32_e32 v67, v64
	v_mov_b32_e32 v68, v64
	v_mov_b32_e32 v69, v64
	v_mov_b32_e32 v70, v64
	v_mov_b32_e32 v71, v64
	v_mov_b32_e32 v72, v64
	v_mov_b32_e32 v73, v64
	v_mov_b32_e32 v74, v64
	v_mov_b32_e32 v75, v64
	v_mov_b32_e32 v76, v64
	v_mov_b32_e32 v77, v64
	v_mov_b32_e32 v78, v64
	v_mov_b32_e32 v79, v64
	v_mov_b32_e32 v80, v64
	v_mov_b32_e32 v81, v64
	v_mov_b32_e32 v82, v64
	v_mov_b32_e32 v83, v64
	v_mov_b32_e32 v84, v64
	v_mov_b32_e32 v85, v64
	v_mov_b32_e32 v86, v64
	v_mov_b32_e32 v87, v64
	v_mov_b32_e32 v88, v64
	v_mov_b32_e32 v89, v64
	v_mov_b32_e32 v90, v64
	v_mov_b32_e32 v91, v64
	v_mov_b32_e32 v92, v64
	v_mov_b32_e32 v93, v64
	v_mov_b32_e32 v94, v64
	v_mov_b32_e32 v95, v64
	s_branch .LBB4_873
